# attention phase: the tail drain of the expert-conversion queue is skipped (each of the 256 workgroups already takes exactly one of the 256 batches, the tail claim always came back empty)
# speedup vs baseline: 1.0082x; 1.0082x over previous
; #define LAS __attribute__((address_space(3)))
; __device__ __forceinline__ KA kargs() { KA p = (KA)__builtin_amdgcn_kernarg_segment_ptr(); asm volatile("" : "+s"(p)); return p; }
; __device__ __forceinline__ void attn_conv_batches(LAS unsigned char* lds, int wv, int l, int max_batches) {
;     const Frame F = make_frame(lds, wv); const KA a = kargs();
;     const int ln = l + 1; unsigned* cq = F.ctl + CW_CVQ + l * 16;
;     const float* w1 = a->in[24] + (size_t)ln * NE * D * DE; const float* w3 = a->in[25] + (size_t)ln * NE * D * DE; const float* w2 = a->in[26] + (size_t)ln * NE * DE * D;
;     unsigned char* WT8 = (unsigned char*)(F.ws + ((ln & 1) ? WS_WTB : WS_WT8)); unsigned char* WT9 = WT8 + 16 * MiB;
;     LAS float* scr = (LAS float*)(F.lds + F.wave * 16384);
; #pragma unroll 1
;     for (int nb = 0; nb < max_batches; ++nb) {
;         int bt;
;         { volatile LAS int* slot = (volatile LAS int*)(lds + MISC_OFF + 512);
;           if (F.tid == 0) *slot = (int)__hip_atomic_fetch_add(cq, 1u, __ATOMIC_RELAXED, __HIP_MEMORY_SCOPE_AGENT);
;           __syncthreads(); bt = *slot; __syncthreads(); }
;         if (bt >= 3 * 2048 / 24) break;
;     ...
;     if (qs == 0 && l + 1 < L) attn_conv_batches(lds, wv, l, 1 << 30);
.LBB0_1092:
	v_readlane_b32 s2, v255, 9
	v_readlane_b32 s3, v255, 10
	s_andn2_b64 vcc, exec, s[2:3]
	s_mov_b32 s24, 0x3fd744fd
	s_branch .LBB0_1112
	v_readlane_b32 s10, v253, 0
	v_readlane_b32 s11, v253, 1
	s_mov_b64 s[2:3], s[10:11]
	s_load_dwordx2 s[14:15], s[2:3], 0xf0
	s_mov_b32 s2, -1
	v_mov_b32_e32 v3, v31
	v_mbcnt_lo_u32_b32 v0, s2, 0
	v_mbcnt_hi_u32_b32 v2, s2, v0
	s_mov_b64 s[2:3], s[10:11]
	v_readlane_b32 s10, v255, 7
	v_readlane_b32 s11, v255, 8
	s_waitcnt lgkmcnt(0)
	s_add_u32 s4, s14, s10
	s_addc_u32 s11, s15, s11
	s_add_u32 s10, s4, 0x2e00
	s_load_dwordx4 s[40:43], s[2:3], 0xc0
	s_load_dwordx2 s[16:17], s[2:3], 0xd0
	s_addc_u32 s11, s11, 0
	s_lshl_b64 s[2:3], s[72:73], 25
	s_add_u32 s4, s2, 0x2000000
	s_addc_u32 s20, s3, 0
	s_waitcnt lgkmcnt(0)
	s_add_u32 s21, s40, s4
	s_addc_u32 s28, s41, s20
	s_add_u32 s2, s42, s4
	s_addc_u32 s3, s43, s20
	s_add_u32 s13, s16, s4
	s_addc_u32 s20, s17, s20
	s_and_b64 s[6:7], s[6:7], exec
	s_mov_b32 s4, 0x1ed00000
	s_cselect_b32 s4, s4, 0xe100000
	s_add_u32 s6, s14, s4
	v_readlane_b32 s4, v253, 8
	v_lshrrev_b32_e32 v1, 5, v2
	v_and_b32_e32 v0, 31, v2
	v_cmp_eq_u32_e64 s[38:39], s4, v2
	v_lshrrev_b32_e32 v10, 3, v2
	v_lshlrev_b32_e32 v2, 3, v2
	s_addc_u32 s7, s15, 0
	v_and_b32_e32 v2, 56, v2
	v_mul_u32_u24_e32 v7, 0x84, v2
	v_lshl_add_u64 v[2:3], s[6:7], 0, v[2:3]
	s_mov_b64 s[6:7], 0x1000000
	v_lshlrev_b32_e32 v8, 2, v10
	v_readlane_b32 s4, v253, 4
	v_lshlrev_b32_e32 v6, 2, v0
	v_lshl_add_u64 v[4:5], v[2:3], 0, s[6:7]
	v_add3_u32 v11, s4, v7, v8
	v_mul_u32_u24_e32 v7, 0x84, v1
	v_readlane_b32 s6, v254, 11
	v_add3_u32 v12, s4, v6, v7
	v_add_u32_e32 v13, 8, v10
	v_add_u32_e32 v6, s6, v10
	v_lshlrev_b32_e32 v7, 1, v6
	v_and_b32_e32 v6, 0x7f, v6
	v_and_or_b32 v16, v7, s0, v6
	v_add_u32_e32 v6, s6, v13
	v_or_b32_e32 v14, 16, v10
	v_lshlrev_b32_e32 v7, 1, v6
	v_and_b32_e32 v6, 0x7f, v6
	v_and_or_b32 v17, v7, s0, v6
	v_add_u32_e32 v6, s6, v14
	v_add_u32_e32 v15, 24, v10
	v_lshlrev_b32_e32 v7, 1, v6
	v_and_b32_e32 v6, 0x7f, v6
	s_lshl_b32 s4, s6, 2
	v_and_or_b32 v18, v7, s0, v6
	v_add_u32_e32 v6, s6, v15
	s_add_u32 s21, s21, s4
	v_lshlrev_b32_e32 v7, 1, v6
	v_and_b32_e32 v6, 0x7f, v6
	v_readlane_b32 s4, v254, 12
	v_and_or_b32 v19, v7, s0, v6
	s_mov_b32 s1, 0
	v_add_u32_e32 v6, s4, v10
	v_lshlrev_b32_e32 v7, 1, v6
	v_and_b32_e32 v6, 0x7f, v6
	v_and_or_b32 v20, v7, s0, v6
	v_add_u32_e32 v6, s4, v13
	v_lshlrev_b32_e32 v7, 1, v6
	v_and_b32_e32 v6, 0x7f, v6
	v_and_or_b32 v21, v7, s0, v6
	v_add_u32_e32 v6, s4, v14
	v_lshlrev_b32_e32 v7, 1, v6
	v_and_b32_e32 v6, 0x7f, v6
	v_and_or_b32 v22, v7, s0, v6
	v_add_u32_e32 v6, s4, v15
	v_lshlrev_b32_e32 v7, 1, v6
	v_and_b32_e32 v6, 0x7f, v6
	s_addc_u32 s28, s28, 0
	v_and_or_b32 v23, v7, s0, v6
	v_readlane_b32 s42, v254, 52
	s_branch .LBB0_1096
